# P0: read-once inputs (f32 expert weights in the transposes, x in the xbf loop) loaded with the nt hint
# speedup vs baseline: 1.0114x; 1.0114x over previous
.LBB0_16:
	v_readfirstlane_b32 s50, v18
	s_lshl_b32 s51, s8, 12
	s_lshl_b32 s50, s50, 2
	s_add_u32 s50, s50, s51
	s_add_u32 s56, s6, s50
	s_addc_u32 s57, s7, 0
	v_and_b32_e32 v100, 3, v36
	v_lshrrev_b32_e32 v101, 5, v36
	v_lshl_or_b32 v100, v101, 2, v100
	v_bfe_u32 v101, v36, 2, 3
	v_lshlrev_b32_e32 v102, 12, v100
	v_lshl_or_b32 v102, v101, 4, v102
	v_lshlrev_b32_e32 v103, 2, v6
	v_sub_u32_e32 v103, v8, v103
	v_mad_u32_u24 v103, v100, s15, v103
	v_lshl_add_u32 v103, v101, 4, v103
	global_load_dwordx4 v[120:123], v102, s[56:57] nt
	s_add_u32 s56, s56, 0x8000
	s_addc_u32 s57, s57, 0
	global_load_dwordx4 v[124:127], v102, s[56:57] nt
	s_add_u32 s56, s56, 0x8000
	s_addc_u32 s57, s57, 0
	s_cmp_lg_u32 s60, 0
	s_cbranch_scc0 .Lnp_dn
	global_store_dwordx4 v[164:165], v[160:163], off
	global_store_dwordx4 v[170:171], v[166:169], off
	s_waitcnt vmcnt(2)
	s_branch .Ljoin_dn

.Ljoin_dn:
	v_pk_mul_f32 v[120:121], v[120:121], s[10:11] op_sel_hi:[1,0]
	v_pk_mul_f32 v[122:123], v[122:123], s[10:11] op_sel_hi:[1,0]
	ds_write_b32 v103, v120 offset:0
	ds_write_b32 v103, v121 offset:4
	ds_write_b32 v103, v122 offset:8
	ds_write_b32 v103, v123 offset:12
	v_pk_mul_f32 v[124:125], v[124:125], s[10:11] op_sel_hi:[1,0]
	v_pk_mul_f32 v[126:127], v[126:127], s[10:11] op_sel_hi:[1,0]
	ds_write_b32 v103, v124 offset:1056
	ds_write_b32 v103, v125 offset:1060
	ds_write_b32 v103, v126 offset:1064
	ds_write_b32 v103, v127 offset:1068
	global_load_dwordx4 v[128:131], v102, s[56:57] nt
	s_add_u32 s56, s56, 0x8000
	s_addc_u32 s57, s57, 0
	global_load_dwordx4 v[132:135], v102, s[56:57] nt
	s_add_u32 s56, s56, 0x8000
	s_addc_u32 s57, s57, 0
	s_waitcnt vmcnt(1)
	v_pk_mul_f32 v[128:129], v[128:129], s[10:11] op_sel_hi:[1,0]
	v_pk_mul_f32 v[130:131], v[130:131], s[10:11] op_sel_hi:[1,0]
	ds_write_b32 v103, v128 offset:2112
	ds_write_b32 v103, v129 offset:2116
	ds_write_b32 v103, v130 offset:2120
	ds_write_b32 v103, v131 offset:2124
	s_waitcnt vmcnt(0)
	v_pk_mul_f32 v[132:133], v[132:133], s[10:11] op_sel_hi:[1,0]
	v_pk_mul_f32 v[134:135], v[134:135], s[10:11] op_sel_hi:[1,0]
	ds_write_b32 v103, v132 offset:3168
	ds_write_b32 v103, v133 offset:3172
	ds_write_b32 v103, v134 offset:3176
	ds_write_b32 v103, v135 offset:3180
	global_load_dwordx4 v[136:139], v102, s[56:57] nt
	s_add_u32 s56, s56, 0x8000
	s_addc_u32 s57, s57, 0
	global_load_dwordx4 v[140:143], v102, s[56:57] nt
	s_add_u32 s56, s56, 0x8000
	s_addc_u32 s57, s57, 0
	s_waitcnt vmcnt(1)
	v_pk_mul_f32 v[136:137], v[136:137], s[10:11] op_sel_hi:[1,0]
	v_pk_mul_f32 v[138:139], v[138:139], s[10:11] op_sel_hi:[1,0]
	ds_write_b32 v103, v136 offset:4224
	ds_write_b32 v103, v137 offset:4228
	ds_write_b32 v103, v138 offset:4232
	ds_write_b32 v103, v139 offset:4236
	s_waitcnt vmcnt(0)
	v_pk_mul_f32 v[140:141], v[140:141], s[10:11] op_sel_hi:[1,0]
	v_pk_mul_f32 v[142:143], v[142:143], s[10:11] op_sel_hi:[1,0]
	ds_write_b32 v103, v140 offset:5280
	ds_write_b32 v103, v141 offset:5284
	ds_write_b32 v103, v142 offset:5288
	ds_write_b32 v103, v143 offset:5292
	global_load_dwordx4 v[144:147], v102, s[56:57] nt
	s_add_u32 s56, s56, 0x8000
	s_addc_u32 s57, s57, 0
	global_load_dwordx4 v[148:151], v102, s[56:57] nt
	s_add_u32 s56, s56, 0x8000
	s_addc_u32 s57, s57, 0
	s_waitcnt vmcnt(1)
	v_pk_mul_f32 v[144:145], v[144:145], s[10:11] op_sel_hi:[1,0]
	v_pk_mul_f32 v[146:147], v[146:147], s[10:11] op_sel_hi:[1,0]
	ds_write_b32 v103, v144 offset:6336
	ds_write_b32 v103, v145 offset:6340
	ds_write_b32 v103, v146 offset:6344
	ds_write_b32 v103, v147 offset:6348
	s_waitcnt vmcnt(0)
	v_pk_mul_f32 v[148:149], v[148:149], s[10:11] op_sel_hi:[1,0]
	v_pk_mul_f32 v[150:151], v[150:151], s[10:11] op_sel_hi:[1,0]
	ds_write_b32 v103, v148 offset:7392
	ds_write_b32 v103, v149 offset:7396
	ds_write_b32 v103, v150 offset:7400
	ds_write_b32 v103, v151 offset:7404
	s_waitcnt lgkmcnt(0)
	v_add_u32_e32 v12, 0x400, v7
	ds_read2_b32 v[22:23], v7 offset1:16
	ds_read2_b32 v[34:35], v7 offset0:33 offset1:49
	ds_read2_b32 v[38:39], v7 offset0:66 offset1:82
	ds_read2_b32 v[40:41], v7 offset0:99 offset1:115
	ds_read2_b32 v[42:43], v7 offset0:132 offset1:148
	ds_read2_b32 v[44:45], v7 offset0:165 offset1:181
	ds_read2_b32 v[46:47], v7 offset0:198 offset1:214
	ds_read2_b32 v[48:49], v7 offset0:231 offset1:247
	ds_read2_b32 v[50:51], v12 offset0:8 offset1:24
	ds_read2_b32 v[52:53], v12 offset0:41 offset1:57
	ds_read2_b32 v[54:55], v12 offset0:74 offset1:90
	ds_read2_b32 v[56:57], v12 offset0:107 offset1:123
	ds_read2_b32 v[58:59], v12 offset0:140 offset1:156
	ds_read2_b32 v[60:61], v12 offset0:173 offset1:189
	s_add_u32 s4, s1, s4
	ds_read2_b32 v[62:63], v12 offset0:206 offset1:222
	ds_read2_b32 v[64:65], v12 offset0:239 offset1:255
	s_addc_u32 s5, s2, s5
	s_lshl_b32 s7, s20, 4
	s_waitcnt lgkmcnt(14)
	v_cvt_pk_fp8_f32 v30, v22, v34
	s_waitcnt lgkmcnt(10)
	v_cvt_pk_fp8_f32 v31, v42, v44
	s_waitcnt lgkmcnt(6)
	v_cvt_pk_fp8_f32 v32, v50, v52
	s_waitcnt lgkmcnt(2)
	v_cvt_pk_fp8_f32 v33, v58, v60
	s_and_b32 s6, s21, 0x300
	s_and_b32 s20, s7, 0x60
	s_add_u32 s4, s4, s8
	v_or_b32_e32 v3, s6, v9
	s_addc_u32 s5, s5, 0
	v_or_b32_e32 v3, s20, v3
	v_lshl_add_u64 v[18:19], s[4:5], 0, v[10:11]
	s_and_b32 s4, s7, 16
	v_cvt_pk_fp8_f32 v30, v38, v40 op_sel:[0,0,1]
	v_cvt_pk_fp8_f32 v31, v46, v48 op_sel:[0,0,1]
	v_cvt_pk_fp8_f32 v32, v54, v56 op_sel:[0,0,1]
	s_waitcnt lgkmcnt(0)
	v_cvt_pk_fp8_f32 v33, v62, v64 op_sel:[0,0,1]
	v_or_b32_e32 v12, s4, v3
	v_lshlrev_b32_e32 v12, 10, v12
	v_lshl_add_u64 v[66:67], v[18:19], 0, v[12:13]
	v_mov_b32_e32 v160, v30
	v_mov_b32_e32 v161, v31
	v_mov_b32_e32 v162, v32
	v_mov_b32_e32 v163, v33
	v_mov_b32_e32 v164, v66
	v_mov_b32_e32 v165, v67
	v_add_u32_e32 v3, s4, v3
	v_lshl_add_u32 v12, v3, 10, v29
	v_cvt_pk_fp8_f32 v30, v23, v35
	v_cvt_pk_fp8_f32 v31, v43, v45
	v_cvt_pk_fp8_f32 v32, v51, v53
	v_cvt_pk_fp8_f32 v33, v59, v61
	v_cvt_pk_fp8_f32 v30, v39, v41 op_sel:[0,0,1]
	v_cvt_pk_fp8_f32 v31, v47, v49 op_sel:[0,0,1]
	v_cvt_pk_fp8_f32 v32, v55, v57 op_sel:[0,0,1]
	v_cvt_pk_fp8_f32 v33, v63, v65 op_sel:[0,0,1]
	v_lshl_add_u64 v[18:19], v[18:19], 0, v[12:13]
	s_mov_b64 s[4:5], 0
	v_mov_b32_e32 v166, v30
	v_mov_b32_e32 v167, v31
	v_mov_b32_e32 v168, v32
	v_mov_b32_e32 v169, v33
	v_mov_b32_e32 v170, v18
	v_mov_b32_e32 v171, v19
	s_mov_b32 s60, 1
	s_waitcnt lgkmcnt(0)

.Lks_done:
	global_load_dwordx4 v[120:123], v102, s[56:57] nt
	s_add_u32 s56, s56, 0x10000
	s_addc_u32 s57, s57, 0
	global_load_dwordx4 v[124:127], v102, s[56:57] nt
	s_add_u32 s56, s56, 0x10000
	s_addc_u32 s57, s57, 0
	s_cmp_lg_u32 s60, 0
	s_cbranch_scc0 .Lnp_gu
	global_store_dwordx4 v[164:165], v[160:163], off
	global_store_dwordx4 v[170:171], v[166:169], off
	s_waitcnt vmcnt(2)
	s_branch .Ljoin_gu

.Ljoin_gu:
	v_pk_mul_f32 v[120:121], v[120:121], s[10:11] op_sel_hi:[1,0]
	v_pk_mul_f32 v[122:123], v[122:123], s[10:11] op_sel_hi:[1,0]
	v_mul_f32_e32 v120, v120, v152
	v_mul_f32_e32 v121, v121, v152
	v_mul_f32_e32 v122, v122, v152
	v_mul_f32_e32 v123, v123, v152
	ds_write_b32 v103, v120 offset:0
	ds_write_b32 v103, v121 offset:4
	ds_write_b32 v103, v122 offset:8
	ds_write_b32 v103, v123 offset:12
	v_pk_mul_f32 v[124:125], v[124:125], s[10:11] op_sel_hi:[1,0]
	v_pk_mul_f32 v[126:127], v[126:127], s[10:11] op_sel_hi:[1,0]
	v_mul_f32_e32 v124, v124, v153
	v_mul_f32_e32 v125, v125, v153
	v_mul_f32_e32 v126, v126, v153
	v_mul_f32_e32 v127, v127, v153
	ds_write_b32 v103, v124 offset:1056
	ds_write_b32 v103, v125 offset:1060
	ds_write_b32 v103, v126 offset:1064
	ds_write_b32 v103, v127 offset:1068
	global_load_dwordx4 v[128:131], v102, s[56:57] nt
	s_add_u32 s56, s56, 0x10000
	s_addc_u32 s57, s57, 0
	global_load_dwordx4 v[132:135], v102, s[56:57] nt
	s_add_u32 s56, s56, 0x10000
	s_addc_u32 s57, s57, 0
	s_waitcnt vmcnt(1)
	v_pk_mul_f32 v[128:129], v[128:129], s[10:11] op_sel_hi:[1,0]
	v_pk_mul_f32 v[130:131], v[130:131], s[10:11] op_sel_hi:[1,0]
	v_mul_f32_e32 v128, v128, v154
	v_mul_f32_e32 v129, v129, v154
	v_mul_f32_e32 v130, v130, v154
	v_mul_f32_e32 v131, v131, v154
	ds_write_b32 v103, v128 offset:2112
	ds_write_b32 v103, v129 offset:2116
	ds_write_b32 v103, v130 offset:2120
	ds_write_b32 v103, v131 offset:2124
	s_waitcnt vmcnt(0)
	v_pk_mul_f32 v[132:133], v[132:133], s[10:11] op_sel_hi:[1,0]
	v_pk_mul_f32 v[134:135], v[134:135], s[10:11] op_sel_hi:[1,0]
	v_mul_f32_e32 v132, v132, v155
	v_mul_f32_e32 v133, v133, v155
	v_mul_f32_e32 v134, v134, v155
	v_mul_f32_e32 v135, v135, v155
	ds_write_b32 v103, v132 offset:3168
	ds_write_b32 v103, v133 offset:3172
	ds_write_b32 v103, v134 offset:3176
	ds_write_b32 v103, v135 offset:3180
	global_load_dwordx4 v[136:139], v102, s[56:57] nt
	s_add_u32 s56, s56, 0x10000
	s_addc_u32 s57, s57, 0
	global_load_dwordx4 v[140:143], v102, s[56:57] nt
	s_add_u32 s56, s56, 0x10000
	s_addc_u32 s57, s57, 0
	s_waitcnt vmcnt(1)
	v_pk_mul_f32 v[136:137], v[136:137], s[10:11] op_sel_hi:[1,0]
	v_pk_mul_f32 v[138:139], v[138:139], s[10:11] op_sel_hi:[1,0]
	v_mul_f32_e32 v136, v136, v156
	v_mul_f32_e32 v137, v137, v156
	v_mul_f32_e32 v138, v138, v156
	v_mul_f32_e32 v139, v139, v156
	ds_write_b32 v103, v136 offset:4224
	ds_write_b32 v103, v137 offset:4228
	ds_write_b32 v103, v138 offset:4232
	ds_write_b32 v103, v139 offset:4236
	s_waitcnt vmcnt(0)
	v_pk_mul_f32 v[140:141], v[140:141], s[10:11] op_sel_hi:[1,0]
	v_pk_mul_f32 v[142:143], v[142:143], s[10:11] op_sel_hi:[1,0]
	v_mul_f32_e32 v140, v140, v157
	v_mul_f32_e32 v141, v141, v157
	v_mul_f32_e32 v142, v142, v157
	v_mul_f32_e32 v143, v143, v157
	ds_write_b32 v103, v140 offset:5280
	ds_write_b32 v103, v141 offset:5284
	ds_write_b32 v103, v142 offset:5288
	ds_write_b32 v103, v143 offset:5292
	global_load_dwordx4 v[144:147], v102, s[56:57] nt
	s_add_u32 s56, s56, 0x10000
	s_addc_u32 s57, s57, 0
	global_load_dwordx4 v[148:151], v102, s[56:57] nt
	s_add_u32 s56, s56, 0x10000
	s_addc_u32 s57, s57, 0
	s_waitcnt vmcnt(1)
	v_pk_mul_f32 v[144:145], v[144:145], s[10:11] op_sel_hi:[1,0]
	v_pk_mul_f32 v[146:147], v[146:147], s[10:11] op_sel_hi:[1,0]
	v_mul_f32_e32 v144, v144, v158
	v_mul_f32_e32 v145, v145, v158
	v_mul_f32_e32 v146, v146, v158
	v_mul_f32_e32 v147, v147, v158
	ds_write_b32 v103, v144 offset:6336
	ds_write_b32 v103, v145 offset:6340
	ds_write_b32 v103, v146 offset:6344
	ds_write_b32 v103, v147 offset:6348
	s_waitcnt vmcnt(0)
	v_pk_mul_f32 v[148:149], v[148:149], s[10:11] op_sel_hi:[1,0]
	v_pk_mul_f32 v[150:151], v[150:151], s[10:11] op_sel_hi:[1,0]
	v_mul_f32_e32 v148, v148, v159
	v_mul_f32_e32 v149, v149, v159
	v_mul_f32_e32 v150, v150, v159
	v_mul_f32_e32 v151, v151, v159
	ds_write_b32 v103, v148 offset:7392
	ds_write_b32 v103, v149 offset:7396
	ds_write_b32 v103, v150 offset:7400
	ds_write_b32 v103, v151 offset:7404
	s_waitcnt lgkmcnt(0)
	v_add_u32_e32 v12, 0x400, v7
	ds_read2_b32 v[22:23], v7 offset1:16
	ds_read2_b32 v[34:35], v7 offset0:33 offset1:49
	ds_read2_b32 v[38:39], v7 offset0:66 offset1:82
	ds_read2_b32 v[40:41], v7 offset0:99 offset1:115
	ds_read2_b32 v[42:43], v7 offset0:132 offset1:148
	ds_read2_b32 v[44:45], v7 offset0:165 offset1:181
	ds_read2_b32 v[46:47], v7 offset0:198 offset1:214
	ds_read2_b32 v[48:49], v7 offset0:231 offset1:247
	ds_read2_b32 v[50:51], v12 offset0:8 offset1:24
	ds_read2_b32 v[52:53], v12 offset0:41 offset1:57
	ds_read2_b32 v[54:55], v12 offset0:74 offset1:90
	ds_read2_b32 v[56:57], v12 offset0:107 offset1:123
	ds_read2_b32 v[58:59], v12 offset0:140 offset1:156
	ds_read2_b32 v[60:61], v12 offset0:173 offset1:189
	s_lshl_b64 s[4:5], s[8:9], 21
	ds_read2_b32 v[62:63], v12 offset0:206 offset1:222
	ds_read2_b32 v[64:65], v12 offset0:239 offset1:255
	s_add_u32 s4, s3, s4
	s_waitcnt lgkmcnt(14)
	v_cvt_pk_fp8_f32 v30, v22, v34
	s_waitcnt lgkmcnt(10)
	v_cvt_pk_fp8_f32 v31, v42, v44
	s_waitcnt lgkmcnt(6)
	v_cvt_pk_fp8_f32 v32, v50, v52
	s_waitcnt lgkmcnt(2)
	v_cvt_pk_fp8_f32 v33, v58, v60
	s_addc_u32 s5, s11, s5
	s_lshl_b32 s8, s20, 6
	s_lshl_b32 s20, s20, 2
	s_and_b32 s8, s8, 0x700
	s_and_b32 s20, s20, 0x80
	s_or_b32 s8, s8, s20
	s_and_b32 s7, s7, 0x60
	s_add_u32 s4, s4, s6
	v_or_b32_e32 v3, s7, v5
	v_cvt_pk_fp8_f32 v30, v38, v40 op_sel:[0,0,1]
	v_cvt_pk_fp8_f32 v31, v46, v48 op_sel:[0,0,1]
	v_cvt_pk_fp8_f32 v32, v54, v56 op_sel:[0,0,1]
	s_waitcnt lgkmcnt(0)
	v_cvt_pk_fp8_f32 v33, v62, v64 op_sel:[0,0,1]
	s_addc_u32 s5, s5, 0
	v_or_b32_e32 v3, s8, v3
	v_lshl_add_u64 v[18:19], s[4:5], 0, v[10:11]
	v_lshlrev_b32_e32 v12, 10, v3
	v_lshl_add_u64 v[66:67], v[18:19], 0, v[12:13]
	v_mov_b32_e32 v160, v30
	v_mov_b32_e32 v161, v31
	v_mov_b32_e32 v162, v32
	v_mov_b32_e32 v163, v33
	v_mov_b32_e32 v164, v66
	v_mov_b32_e32 v165, v67
	v_or_b32_e32 v3, s7, v21
	v_or_b32_e32 v3, s8, v3
	v_cvt_pk_fp8_f32 v30, v23, v35
	v_cvt_pk_fp8_f32 v31, v43, v45
	v_cvt_pk_fp8_f32 v32, v51, v53
	v_cvt_pk_fp8_f32 v33, v59, v61
	v_cvt_pk_fp8_f32 v30, v39, v41 op_sel:[0,0,1]
	v_cvt_pk_fp8_f32 v31, v47, v49 op_sel:[0,0,1]
	v_cvt_pk_fp8_f32 v32, v55, v57 op_sel:[0,0,1]
	v_cvt_pk_fp8_f32 v33, v63, v65 op_sel:[0,0,1]
	v_lshlrev_b32_e32 v12, 10, v3
	v_lshl_add_u64 v[18:19], v[18:19], 0, v[12:13]
	v_mov_b32_e32 v166, v30
	v_mov_b32_e32 v167, v31
	v_mov_b32_e32 v168, v32
	v_mov_b32_e32 v169, v33
	v_mov_b32_e32 v170, v18
	v_mov_b32_e32 v171, v19
	s_mov_b32 s60, 1
	s_waitcnt lgkmcnt(0)

.LBB0_53:
	s_waitcnt lgkmcnt(0)
	global_load_dwordx4 v[16:19], v[6:7], off offset:-2048 nt
	global_load_dwordx4 v[20:23], v[6:7], off offset:-1024 nt
	global_load_dwordx4 v[24:27], v[6:7], off nt
	global_load_dwordx4 v[28:31], v[6:7], off offset:1024 nt
	v_lshl_add_u64 v[32:33], s[12:13], 0, v[2:3]
	v_add_co_u32_e32 v32, vcc, s15, v32
	s_waitcnt vmcnt(3)
	v_mul_f32_e32 v15, v17, v17
	s_waitcnt vmcnt(2)
	v_mul_f32_e32 v34, v21, v21
	s_waitcnt vmcnt(1)
	v_mul_f32_e32 v35, v25, v25
	v_fmac_f32_e32 v34, v20, v20
	v_fmac_f32_e32 v15, v16, v16
	s_waitcnt vmcnt(0)
	v_mul_f32_e32 v36, v29, v29
	v_fmac_f32_e32 v35, v24, v24
	v_fmac_f32_e32 v34, v22, v22
	v_fmac_f32_e32 v15, v18, v18
	v_bfe_u32 v37, v16, 16, 1
	v_bfe_u32 v38, v17, 16, 1
	v_bfe_u32 v39, v18, 16, 1
	v_fmac_f32_e32 v36, v28, v28
	v_fmac_f32_e32 v35, v26, v26
	v_fmac_f32_e32 v34, v23, v23
	v_fmac_f32_e32 v15, v19, v19
	v_bfe_u32 v40, v19, 16, 1
	v_bfe_u32 v41, v20, 16, 1
	v_bfe_u32 v43, v22, 16, 1
	v_add3_u32 v37, v16, v37, s2
	v_add3_u32 v17, v17, v38, s2
	v_add3_u32 v38, v18, v39, s2
	v_fmac_f32_e32 v36, v30, v30
	v_fmac_f32_e32 v35, v27, v27
	v_add_f32_e32 v15, v15, v34
	v_bfe_u32 v42, v21, 16, 1
	v_bfe_u32 v44, v23, 16, 1
	v_add3_u32 v39, v19, v40, s2
	v_add3_u32 v20, v20, v41, s2
	v_add3_u32 v40, v22, v43, s2
	v_lshrrev_b32_e32 v16, 16, v37
	v_lshrrev_b32_e32 v22, 16, v38
	v_fmac_f32_e32 v36, v31, v31
	v_add_f32_e32 v15, v15, v35
	v_addc_co_u32_e32 v33, vcc, 0, v33, vcc
	v_add3_u32 v21, v21, v42, s2
	v_add3_u32 v41, v23, v44, s2
	v_lshrrev_b32_e32 v20, 16, v20
	v_lshrrev_b32_e32 v37, 16, v40
	v_and_or_b32 v16, v17, s3, v16
	v_and_or_b32 v17, v39, s3, v22
	v_add_f32_e32 v15, v15, v36
	v_and_or_b32 v20, v21, s3, v20
	v_and_or_b32 v21, v41, s3, v37
	global_store_dwordx2 v[32:33], v[16:17], off
	global_store_dwordx2 v[32:33], v[20:21], off offset:512
	ds_bpermute_b32 v17, v8, v15
	v_bfe_u32 v45, v24, 16, 1
	v_add3_u32 v24, v24, v45, s2
	v_bfe_u32 v18, v25, 16, 1
	v_lshrrev_b32_e32 v16, 16, v24
	s_waitcnt lgkmcnt(0)
	v_add_f32_e32 v15, v15, v17
	ds_bpermute_b32 v17, v9, v15
	v_add3_u32 v18, v25, v18, s2
	v_and_or_b32 v16, v18, s3, v16
	v_bfe_u32 v18, v26, 16, 1
	v_add3_u32 v18, v26, v18, s2
	s_waitcnt lgkmcnt(0)
	v_add_f32_e32 v15, v15, v17
	ds_bpermute_b32 v20, v10, v15
	v_bfe_u32 v19, v27, 16, 1
	v_lshrrev_b32_e32 v18, 16, v18
	v_add3_u32 v17, v27, v19, s2
	v_and_or_b32 v17, v17, s3, v18
	s_waitcnt lgkmcnt(0)
	v_add_f32_e32 v15, v15, v20
	global_store_dwordx2 v[32:33], v[16:17], off offset:1024
	ds_bpermute_b32 v17, v11, v15
	v_bfe_u32 v16, v28, 16, 1
	v_add3_u32 v16, v28, v16, s2
	v_bfe_u32 v18, v29, 16, 1
	v_lshrrev_b32_e32 v16, 16, v16
	s_waitcnt lgkmcnt(0)
	v_add_f32_e32 v15, v15, v17
	ds_bpermute_b32 v17, v12, v15
	v_add3_u32 v18, v29, v18, s2
	v_and_or_b32 v18, v18, s3, v16
	v_bfe_u32 v16, v30, 16, 1
	v_add3_u32 v16, v30, v16, s2
	s_waitcnt lgkmcnt(0)
	v_add_f32_e32 v15, v15, v17
	v_lshrrev_b32_e32 v19, 16, v16
	ds_bpermute_b32 v16, v13, v15
	v_bfe_u32 v17, v31, 16, 1
	v_add3_u32 v17, v31, v17, s2
	v_and_or_b32 v19, v17, s3, v19
	global_store_dwordx2 v[32:33], v[18:19], off offset:1536
	s_and_saveexec_b64 s[18:19], s[4:5]
	s_cbranch_execz .LBB0_52
	s_waitcnt lgkmcnt(0)
	v_add_f32_e32 v15, v15, v16
	v_fmamk_f32 v15, v15, 0x3a800000, v4
	v_mul_f32_e32 v16, 0x4f800000, v15
	v_cmp_gt_f32_e32 vcc, s20, v15
	s_nop 1
	v_cndmask_b32_e32 v15, v15, v16, vcc
	v_sqrt_f32_e32 v16, v15
	s_nop 0
	v_add_u32_e32 v17, -1, v16
	v_fma_f32 v19, -v17, v16, v15
	v_add_u32_e32 v18, 1, v16
	v_cmp_ge_f32_e64 s[6:7], 0, v19
	s_nop 1
	v_cndmask_b32_e64 v17, v16, v17, s[6:7]
	v_fma_f32 v16, -v18, v16, v15
	v_cmp_lt_f32_e64 s[6:7], 0, v16
	s_nop 1
	v_cndmask_b32_e64 v16, v17, v18, s[6:7]
	v_mul_f32_e32 v17, 0x37800000, v16
	v_cndmask_b32_e32 v16, v16, v17, vcc
	v_cmp_class_f32_e32 vcc, v15, v14
	s_nop 1
	v_cndmask_b32_e32 v15, v16, v15, vcc
	v_div_scale_f32 v16, s[6:7], v15, v15, 1.0
	v_rcp_f32_e32 v17, v16
	s_add_u32 s6, s12, s0
	s_addc_u32 s7, s13, s1
	v_fma_f32 v18, -v16, v17, 1.0
	v_fmac_f32_e32 v17, v18, v17
	v_div_scale_f32 v18, vcc, 1.0, v15, 1.0
	v_mul_f32_e32 v19, v18, v17
	v_fma_f32 v20, -v16, v19, v18
	v_fmac_f32_e32 v19, v20, v17
	v_fma_f32 v16, -v16, v19, v18
	v_div_fmas_f32 v16, v16, v17, v19
	v_div_fixup_f32 v15, v16, v15, 1.0
	global_store_dword v5, v15, s[6:7]
	s_branch .LBB0_52
